# P9: per-unit gather-offset block skipped when the next unit has the same row block (same tokens)
# speedup vs baseline: 1.0054x; 1.0054x over previous
.LBB0_996:
	s_andn2_b64 vcc, exec, s[26:27]
	v_mov_b32_e32 v205, v182
	v_mov_b32_e32 v168, v176
	v_mov_b32_e32 v206, v178
	v_mov_b32_e32 v207, v180
	s_cmp_eq_u32 s18, s22
	s_cbranch_scc1 .LBB0_1006
	s_cbranch_vccnz .LBB0_1006
	v_mov_b32_e32 v242, 0
	v_mov_b32_e32 v243, 0
	v_mov_b32_e32 v244, 0
	v_mov_b32_e32 v245, 0
	s_ashr_i32 s2, s19, 31
	s_lshr_b32 s2, s2, 28
	s_add_i32 s2, s19, s2
	s_ashr_i32 s2, s2, 4
	s_lshl_b32 s3, s2, 2
	s_add_i32 s3, s3, 0
	s_add_i32 s3, s3, 0x20100
	v_mov_b32_e32 v2, s3
	ds_read2st64_b32 v[16:17], v2 offset1:1
	s_lshl_b32 s20, s2, 6
	s_add_i32 s28, s20, 0
	s_lshl_b32 s3, s18, 8
	s_add_i32 s28, s28, 0x20300
	s_waitcnt lgkmcnt(0)
	v_sub_u32_e32 v18, s3, v16
	v_mov_b32_e32 v16, s28
	ds_read2_b32 v[14:15], v16 offset0:1 offset1:2
	ds_read2_b32 v[12:13], v16 offset0:3 offset1:4
	ds_read2_b32 v[10:11], v16 offset0:5 offset1:6
	ds_read2_b32 v[8:9], v16 offset0:7 offset1:8
	ds_read2_b32 v[6:7], v16 offset0:9 offset1:10
	ds_read2_b32 v[4:5], v16 offset0:11 offset1:12
	ds_read2_b32 v[2:3], v16 offset0:13 offset1:14
	ds_read_b32 v16, v16 offset:60
	v_add_u32_e32 v19, v18, v162
	s_ashr_i32 s3, s2, 31
	s_lshl_b64 s[20:21], s[2:3], 4
	v_cmp_lt_i32_e32 vcc, v19, v17
	v_mov_b32_e32 v21, 0
	v_mov_b32_e32 v20, 0
	s_and_saveexec_b64 s[2:3], vcc
	s_cbranch_execz .LBB0_999
	s_waitcnt lgkmcnt(0)
	v_cmp_le_i32_e32 vcc, v14, v19
	s_nop 1
	v_cndmask_b32_e64 v20, 0, 1, vcc
	v_cmp_le_i32_e32 vcc, v15, v19
	s_nop 1
	v_cndmask_b32_e64 v22, 0, 1, vcc
	v_cmp_le_i32_e32 vcc, v12, v19
	s_nop 1
	v_addc_co_u32_e32 v20, vcc, v20, v22, vcc
	v_cmp_le_i32_e32 vcc, v13, v19
	s_nop 1
	v_cndmask_b32_e64 v22, 0, 1, vcc
	v_cmp_le_i32_e32 vcc, v10, v19
	s_nop 1
	v_addc_co_u32_e32 v20, vcc, v20, v22, vcc
	v_cmp_le_i32_e32 vcc, v11, v19
	s_nop 1
	v_cndmask_b32_e64 v22, 0, 1, vcc
	v_cmp_le_i32_e32 vcc, v8, v19
	s_nop 1
	v_addc_co_u32_e32 v20, vcc, v20, v22, vcc
	v_cmp_le_i32_e32 vcc, v9, v19
	s_nop 1
	v_cndmask_b32_e64 v22, 0, 1, vcc
	v_cmp_le_i32_e32 vcc, v6, v19
	s_nop 1
	v_addc_co_u32_e32 v20, vcc, v20, v22, vcc
	v_cmp_le_i32_e32 vcc, v7, v19
	s_nop 1
	v_cndmask_b32_e64 v22, 0, 1, vcc
	v_cmp_le_i32_e32 vcc, v4, v19
	s_nop 1
	v_addc_co_u32_e32 v20, vcc, v20, v22, vcc
	v_cmp_le_i32_e32 vcc, v5, v19
	s_nop 1
	v_cndmask_b32_e64 v22, 0, 1, vcc
	v_cmp_le_i32_e32 vcc, v2, v19
	s_nop 1
	v_addc_co_u32_e32 v20, vcc, v20, v22, vcc
	v_cmp_le_i32_e32 vcc, v3, v19
	s_nop 1
	v_cndmask_b32_e64 v22, 0, 1, vcc
	v_cmp_le_i32_e32 vcc, v16, v19
	s_nop 1
	v_addc_co_u32_e32 v168, vcc, v20, v22, vcc
	v_lshl_add_u32 v20, v168, 2, s28
	ds_read_b32 v20, v20
	v_lshl_add_u64 v[22:23], s[20:21], 0, v[168:169]
	v_lshlrev_b64 v[22:23], 13, v[22:23]
	v_lshl_add_u64 v[22:23], s[0:1], 0, v[22:23]
	s_waitcnt lgkmcnt(0)
	v_sub_u32_e32 v24, v19, v20
	v_ashrrev_i32_e32 v25, 31, v24
	v_lshl_add_u64 v[22:23], v[24:25], 2, v[22:23]
	global_load_dword v242, v[22:23], off
